# st64 + combine_final: issue all 24 x/a/b loads of a token together (counted vmcnt) instead of 8 serialized round trips
# speedup vs baseline: 1.0107x; 1.0020x over previous
.LBB6_2021:
	v_lshl_add_u64 v[36:37], s[38:39], 0, v[72:73]
	s_mov_b64 s[0:1], 0x26400000
	v_lshl_add_u64 v[40:41], v[36:37], 0, s[0:1]
	v_add_co_u32_e32 v36, vcc, 0x26400000, v36
	s_mov_b32 s0, 0x200000
	s_nop 0
	v_addc_co_u32_e32 v37, vcc, 0, v37, vcc
	global_load_dwordx4 v[36:39], v[36:37], off
	s_nop 0
	global_load_dwordx2 v[74:75], v[40:41], off offset:16
	v_add_u32_e32 v68, s6, v68
	v_lshl_add_u64 v[72:73], v[72:73], 0, s[18:19]
	s_waitcnt vmcnt(0)
	v_ashrrev_i32_e32 v41, 31, v36
	v_mov_b32_e32 v40, v36
	v_ashrrev_i32_e32 v43, 31, v37
	v_mov_b32_e32 v42, v37
	v_lshlrev_b64 v[36:37], 25, v[40:41]
	v_lshl_add_u64 v[36:37], s[12:13], 0, v[36:37]
	v_lshlrev_b64 v[40:41], 12, v[42:43]
	v_lshl_add_u64 v[36:37], v[36:37], 0, v[40:41]
	v_ashrrev_i32_e32 v41, 31, v39
	v_mov_b32_e32 v40, v39
	v_ashrrev_i32_e32 v43, 31, v74
	v_mov_b32_e32 v42, v74
	v_lshlrev_b64 v[40:41], 25, v[40:41]
	v_lshl_add_u64 v[40:41], s[12:13], 0, v[40:41]
	v_lshlrev_b64 v[42:43], 12, v[42:43]
	v_lshl_add_u64 v[40:41], v[40:41], 0, v[42:43]
	v_lshl_add_u64 v[42:43], s[38:39], 0, v[70:71]
	v_add_co_u32_e32 v152, vcc, s0, v42
	v_lshl_add_u64 v[156:157], v[36:37], 0, v[2:3]
	s_nop 0
	v_addc_co_u32_e32 v153, vcc, 0, v43, vcc
	v_add_co_u32_e32 v154, vcc, s14, v42
	v_lshl_add_u64 v[158:159], v[40:41], 0, v[2:3]
	s_nop 0
	v_addc_co_u32_e32 v155, vcc, 0, v43, vcc
	s_nop 1
	global_load_dwordx4 v[144:147], v[152:153], off
	global_load_dwordx4 v[40:43], v[152:153], off offset:1024
	global_load_dwordx4 v[44:47], v[152:153], off offset:2048
	global_load_dwordx4 v[48:51], v[152:153], off offset:3072
	global_load_dwordx4 v[52:55], v[154:155], off
	global_load_dwordx4 v[60:63], v[154:155], off offset:1024
	global_load_dwordx4 v[56:59], v[154:155], off offset:2048
	global_load_dwordx4 v[64:67], v[154:155], off offset:3072
	global_load_dwordx2 v[160:161], v[156:157], off
	global_load_dwordx2 v[184:185], v[158:159], off
	global_load_dwordx2 v[162:163], v[156:157], off offset:512
	global_load_dwordx2 v[186:187], v[158:159], off offset:512
	global_load_dwordx2 v[164:165], v[156:157], off offset:1024
	global_load_dwordx2 v[188:189], v[158:159], off offset:1024
	global_load_dwordx2 v[166:167], v[156:157], off offset:1536
	global_load_dwordx2 v[190:191], v[158:159], off offset:1536
	global_load_dwordx2 v[168:169], v[156:157], off offset:2048
	global_load_dwordx2 v[192:193], v[158:159], off offset:2048
	global_load_dwordx2 v[170:171], v[156:157], off offset:2560
	global_load_dwordx2 v[194:195], v[158:159], off offset:2560
	global_load_dwordx2 v[172:173], v[156:157], off offset:3072
	global_load_dwordx2 v[196:197], v[158:159], off offset:3072
	global_load_dwordx2 v[174:175], v[156:157], off offset:3584
	global_load_dwordx2 v[198:199], v[158:159], off offset:3584
	s_waitcnt vmcnt(14)
	v_lshlrev_b32_e32 v78, 16, v160
	v_and_b32_e32 v79, 0xffff0000, v160
	v_lshlrev_b32_e32 v80, 16, v161
	v_and_b32_e32 v81, 0xffff0000, v161
	v_lshlrev_b32_e32 v82, 16, v184
	v_and_b32_e32 v83, 0xffff0000, v184
	v_lshlrev_b32_e32 v84, 16, v185
	v_and_b32_e32 v85, 0xffff0000, v185
	v_pk_fma_f32 v[36:37], v[38:39], v[78:79], v[144:145] op_sel_hi:[0,1,1]
	v_pk_fma_f32 v[76:77], v[38:39], v[80:81], v[146:147] op_sel_hi:[0,1,1]
	v_pk_fma_f32 v[36:37], v[74:75], v[82:83], v[36:37] op_sel:[1,0,0]
	v_pk_fma_f32 v[76:77], v[74:75], v[84:85], v[76:77] op_sel:[1,0,0]
	v_pk_mul_f32 v[90:91], v[36:37], v[36:37]
	v_pk_fma_f32 v[90:91], v[76:77], v[76:77], v[90:91]
	s_waitcnt vmcnt(12)
	v_lshlrev_b32_e32 v78, 16, v162
	v_and_b32_e32 v79, 0xffff0000, v162
	v_lshlrev_b32_e32 v80, 16, v163
	v_and_b32_e32 v81, 0xffff0000, v163
	v_lshlrev_b32_e32 v82, 16, v186
	v_and_b32_e32 v83, 0xffff0000, v186
	v_lshlrev_b32_e32 v84, 16, v187
	v_and_b32_e32 v85, 0xffff0000, v187
	v_pk_fma_f32 v[40:41], v[38:39], v[78:79], v[40:41] op_sel_hi:[0,1,1]
	v_pk_fma_f32 v[42:43], v[38:39], v[80:81], v[42:43] op_sel_hi:[0,1,1]
	v_pk_fma_f32 v[40:41], v[74:75], v[82:83], v[40:41] op_sel:[1,0,0]
	v_pk_fma_f32 v[42:43], v[74:75], v[84:85], v[42:43] op_sel:[1,0,0]
	v_pk_fma_f32 v[90:91], v[40:41], v[40:41], v[90:91]
	v_pk_fma_f32 v[90:91], v[42:43], v[42:43], v[90:91]
	s_waitcnt vmcnt(10)
	v_lshlrev_b32_e32 v78, 16, v164
	v_and_b32_e32 v79, 0xffff0000, v164
	v_lshlrev_b32_e32 v80, 16, v165
	v_and_b32_e32 v81, 0xffff0000, v165
	v_lshlrev_b32_e32 v82, 16, v188
	v_and_b32_e32 v83, 0xffff0000, v188
	v_lshlrev_b32_e32 v84, 16, v189
	v_and_b32_e32 v85, 0xffff0000, v189
	v_pk_fma_f32 v[44:45], v[38:39], v[78:79], v[44:45] op_sel_hi:[0,1,1]
	v_pk_fma_f32 v[46:47], v[38:39], v[80:81], v[46:47] op_sel_hi:[0,1,1]
	v_pk_fma_f32 v[44:45], v[74:75], v[82:83], v[44:45] op_sel:[1,0,0]
	v_pk_fma_f32 v[46:47], v[74:75], v[84:85], v[46:47] op_sel:[1,0,0]
	v_pk_fma_f32 v[90:91], v[44:45], v[44:45], v[90:91]
	v_pk_fma_f32 v[90:91], v[46:47], v[46:47], v[90:91]
	s_waitcnt vmcnt(8)
	v_lshlrev_b32_e32 v78, 16, v166
	v_and_b32_e32 v79, 0xffff0000, v166
	v_lshlrev_b32_e32 v80, 16, v167
	v_and_b32_e32 v81, 0xffff0000, v167
	v_lshlrev_b32_e32 v82, 16, v190
	v_and_b32_e32 v83, 0xffff0000, v190
	v_lshlrev_b32_e32 v84, 16, v191
	v_and_b32_e32 v85, 0xffff0000, v191
	v_pk_fma_f32 v[48:49], v[38:39], v[78:79], v[48:49] op_sel_hi:[0,1,1]
	v_pk_fma_f32 v[50:51], v[38:39], v[80:81], v[50:51] op_sel_hi:[0,1,1]
	v_pk_fma_f32 v[48:49], v[74:75], v[82:83], v[48:49] op_sel:[1,0,0]
	v_pk_fma_f32 v[50:51], v[74:75], v[84:85], v[50:51] op_sel:[1,0,0]
	v_pk_fma_f32 v[90:91], v[48:49], v[48:49], v[90:91]
	v_pk_fma_f32 v[90:91], v[50:51], v[50:51], v[90:91]
	s_waitcnt vmcnt(6)
	v_lshlrev_b32_e32 v78, 16, v168
	v_and_b32_e32 v79, 0xffff0000, v168
	v_lshlrev_b32_e32 v80, 16, v169
	v_and_b32_e32 v81, 0xffff0000, v169
	v_lshlrev_b32_e32 v82, 16, v192
	v_and_b32_e32 v83, 0xffff0000, v192
	v_lshlrev_b32_e32 v84, 16, v193
	v_and_b32_e32 v85, 0xffff0000, v193
	v_pk_fma_f32 v[52:53], v[38:39], v[78:79], v[52:53] op_sel_hi:[0,1,1]
	v_pk_fma_f32 v[54:55], v[38:39], v[80:81], v[54:55] op_sel_hi:[0,1,1]
	v_pk_fma_f32 v[52:53], v[74:75], v[82:83], v[52:53] op_sel:[1,0,0]
	v_pk_fma_f32 v[54:55], v[74:75], v[84:85], v[54:55] op_sel:[1,0,0]
	v_pk_fma_f32 v[90:91], v[52:53], v[52:53], v[90:91]
	v_pk_fma_f32 v[90:91], v[54:55], v[54:55], v[90:91]
	s_waitcnt vmcnt(4)
	v_lshlrev_b32_e32 v78, 16, v170
	v_and_b32_e32 v79, 0xffff0000, v170
	v_lshlrev_b32_e32 v80, 16, v171
	v_and_b32_e32 v81, 0xffff0000, v171
	v_lshlrev_b32_e32 v82, 16, v194
	v_and_b32_e32 v83, 0xffff0000, v194
	v_lshlrev_b32_e32 v84, 16, v195
	v_and_b32_e32 v85, 0xffff0000, v195
	v_pk_fma_f32 v[60:61], v[38:39], v[78:79], v[60:61] op_sel_hi:[0,1,1]
	v_pk_fma_f32 v[62:63], v[38:39], v[80:81], v[62:63] op_sel_hi:[0,1,1]
	v_pk_fma_f32 v[60:61], v[74:75], v[82:83], v[60:61] op_sel:[1,0,0]
	v_pk_fma_f32 v[62:63], v[74:75], v[84:85], v[62:63] op_sel:[1,0,0]
	v_pk_fma_f32 v[90:91], v[60:61], v[60:61], v[90:91]
	v_pk_fma_f32 v[90:91], v[62:63], v[62:63], v[90:91]
	s_waitcnt vmcnt(2)
	v_lshlrev_b32_e32 v78, 16, v172
	v_and_b32_e32 v79, 0xffff0000, v172
	v_lshlrev_b32_e32 v80, 16, v173
	v_and_b32_e32 v81, 0xffff0000, v173
	v_lshlrev_b32_e32 v82, 16, v196
	v_and_b32_e32 v83, 0xffff0000, v196
	v_lshlrev_b32_e32 v84, 16, v197
	v_and_b32_e32 v85, 0xffff0000, v197
	v_pk_fma_f32 v[56:57], v[38:39], v[78:79], v[56:57] op_sel_hi:[0,1,1]
	v_pk_fma_f32 v[58:59], v[38:39], v[80:81], v[58:59] op_sel_hi:[0,1,1]
	v_pk_fma_f32 v[56:57], v[74:75], v[82:83], v[56:57] op_sel:[1,0,0]
	v_pk_fma_f32 v[58:59], v[74:75], v[84:85], v[58:59] op_sel:[1,0,0]
	v_pk_fma_f32 v[90:91], v[56:57], v[56:57], v[90:91]
	v_pk_fma_f32 v[90:91], v[58:59], v[58:59], v[90:91]
	s_waitcnt vmcnt(0)
	v_lshlrev_b32_e32 v78, 16, v174
	v_and_b32_e32 v79, 0xffff0000, v174
	v_lshlrev_b32_e32 v80, 16, v175
	v_and_b32_e32 v81, 0xffff0000, v175
	v_lshlrev_b32_e32 v82, 16, v198
	v_and_b32_e32 v83, 0xffff0000, v198
	v_lshlrev_b32_e32 v84, 16, v199
	v_and_b32_e32 v85, 0xffff0000, v199
	v_pk_fma_f32 v[64:65], v[38:39], v[78:79], v[64:65] op_sel_hi:[0,1,1]
	v_pk_fma_f32 v[66:67], v[38:39], v[80:81], v[66:67] op_sel_hi:[0,1,1]
	v_pk_fma_f32 v[64:65], v[74:75], v[82:83], v[64:65] op_sel:[1,0,0]
	v_pk_fma_f32 v[66:67], v[74:75], v[84:85], v[66:67] op_sel:[1,0,0]
	v_pk_fma_f32 v[90:91], v[64:65], v[64:65], v[90:91]
	v_pk_fma_f32 v[90:91], v[66:67], v[66:67], v[90:91]
	s_nop 0
	v_add_f32_e32 v38, v90, v91
	ds_bpermute_b32 v39, v138, v38
	v_lshl_add_u64 v[144:145], s[10:11], 0, v[70:71]
	v_lshl_add_u64 v[70:71], v[70:71], 0, s[16:17]
	s_waitcnt lgkmcnt(0)
	v_add_f32_e32 v38, v38, v39
	ds_bpermute_b32 v39, v139, v38
	s_waitcnt lgkmcnt(0)
	v_add_f32_e32 v38, v38, v39
	ds_bpermute_b32 v39, v140, v38
	s_waitcnt lgkmcnt(0)
	v_add_f32_e32 v38, v38, v39
	ds_bpermute_b32 v39, v141, v38
	s_waitcnt lgkmcnt(0)
	v_add_f32_e32 v38, v38, v39
	ds_bpermute_b32 v39, v142, v38
	s_waitcnt lgkmcnt(0)
	v_add_f32_e32 v38, v38, v39
	ds_bpermute_b32 v39, v143, v38
	s_waitcnt lgkmcnt(0)
	v_add_f32_e32 v38, v38, v39
	v_fmamk_f32 v38, v38, 0x3a000000, v212
	v_cmp_gt_f32_e32 vcc, s58, v38
	v_mul_f32_e32 v39, 0x4b800000, v38
	s_nop 0
	v_cndmask_b32_e32 v38, v38, v39, vcc
	v_rsq_f32_e32 v38, v38
	s_nop 0
	v_mul_f32_e32 v39, 0x45800000, v38
	v_cndmask_b32_e32 v74, v38, v39, vcc
	v_pk_mul_f32 v[36:37], v[36:37], v[74:75] op_sel_hi:[1,0]
	v_pk_mul_f32 v[38:39], v[76:77], v[74:75] op_sel_hi:[1,0]
	v_pk_mul_f32 v[36:37], v[4:5], v[36:37]
	v_pk_mul_f32 v[38:39], v[6:7], v[38:39]
	global_store_dwordx4 v[144:145], v[36:39], off
	s_nop 1
	v_pk_mul_f32 v[36:37], v[40:41], v[74:75] op_sel_hi:[1,0]
	v_pk_mul_f32 v[38:39], v[42:43], v[74:75] op_sel_hi:[1,0]
	v_pk_mul_f32 v[36:37], v[8:9], v[36:37]
	v_pk_mul_f32 v[38:39], v[10:11], v[38:39]
	global_store_dwordx4 v[144:145], v[36:39], off offset:1024
	v_add_co_u32_e32 v40, vcc, s33, v144
	s_nop 0
	v_pk_mul_f32 v[36:37], v[44:45], v[74:75] op_sel_hi:[1,0]
	v_pk_mul_f32 v[38:39], v[46:47], v[74:75] op_sel_hi:[1,0]
	v_pk_mul_f32 v[36:37], v[12:13], v[36:37]
	v_pk_mul_f32 v[38:39], v[14:15], v[38:39]
	global_store_dwordx4 v[144:145], v[36:39], off offset:2048
	v_addc_co_u32_e32 v41, vcc, 0, v145, vcc
	s_nop 0
	v_pk_mul_f32 v[36:37], v[48:49], v[74:75] op_sel_hi:[1,0]
	v_pk_mul_f32 v[38:39], v[50:51], v[74:75] op_sel_hi:[1,0]
	v_pk_mul_f32 v[36:37], v[16:17], v[36:37]
	v_pk_mul_f32 v[38:39], v[18:19], v[38:39]
	global_store_dwordx4 v[144:145], v[36:39], off offset:3072
	v_cmp_lt_i32_e32 vcc, s7, v68
	s_or_b64 s[4:5], vcc, s[4:5]
	v_pk_mul_f32 v[36:37], v[52:53], v[74:75] op_sel_hi:[1,0]
	v_pk_mul_f32 v[38:39], v[54:55], v[74:75] op_sel_hi:[1,0]
	v_pk_mul_f32 v[36:37], v[20:21], v[36:37]
	v_pk_mul_f32 v[38:39], v[22:23], v[38:39]
	global_store_dwordx4 v[40:41], v[36:39], off
	s_nop 1
	v_pk_mul_f32 v[36:37], v[60:61], v[74:75] op_sel_hi:[1,0]
	v_pk_mul_f32 v[38:39], v[62:63], v[74:75] op_sel_hi:[1,0]
	v_pk_mul_f32 v[36:37], v[24:25], v[36:37]
	v_pk_mul_f32 v[38:39], v[26:27], v[38:39]
	global_store_dwordx4 v[40:41], v[36:39], off offset:1024
	s_nop 1
	v_pk_mul_f32 v[36:37], v[56:57], v[74:75] op_sel_hi:[1,0]
	v_pk_mul_f32 v[38:39], v[58:59], v[74:75] op_sel_hi:[1,0]
	v_pk_mul_f32 v[36:37], v[28:29], v[36:37]
	v_pk_mul_f32 v[38:39], v[30:31], v[38:39]
	global_store_dwordx4 v[40:41], v[36:39], off offset:2048
	s_nop 1
	v_pk_mul_f32 v[36:37], v[64:65], v[74:75] op_sel_hi:[1,0]
	v_pk_mul_f32 v[38:39], v[66:67], v[74:75] op_sel_hi:[1,0]
	v_pk_mul_f32 v[36:37], v[32:33], v[36:37]
	v_pk_mul_f32 v[38:39], v[34:35], v[38:39]
	global_store_dwordx4 v[40:41], v[36:39], off offset:3072
	s_andn2_b64 exec, exec, s[4:5]
	s_cbranch_execnz .LBB6_2021
